# v82: v79 + gdn_gb staging waves rewritten with three register sets (operands requested three step intervals ahead), SGPR-base addressing
# speedup vs baseline: 1.0028x; 1.0028x over previous
.LBB0_1639:
	s_waitcnt vmcnt(0)
	s_lshl_b32 s42, s3, 1
	s_or_b32 s42, s42, s39
	s_lshl_b32 s52, s38, 10
	s_or_b32 s52, s52, s42
	s_lshl_b32 s43, s38, 6
	s_add_i32 s43, s43, 0x1000
	s_or_b32 s43, s43, s42
	s_cmp_eq_u32 s39, 0
	s_cselect_b32 s8, 0, 0x470
	s_cselect_b32 s25, 0, 48
	s_cselect_b32 s42, 16, -16
	s_add_i32 s52, s52, s8
	s_sub_u32 s52, s52, 64
	s_add_i32 s43, s43, s25
	v_and_b32_e32 v15, 63, v176
	s_lshl_b32 s8, s35, 12
	v_lshlrev_b32_e32 v4, 4, v15
	s_lshl_b32 s9, s35, 11
	v_add_u32_e32 v5, s9, v4
	v_lshrrev_b32_e32 v13, 3, v15
	v_and_b32_e32 v14, 7, v15
	s_lshl_b32 s25, s2, 1
	v_lshlrev_b32_e32 v6, 8, v13
	v_lshl_add_u32 v6, v14, 4, v6
	s_add_i32 s25, s25, s8
	v_add_u32_e32 v6, s25, v6
	v_add_u32_e32 v4, s8, v4
	s_lshl_b32 s25, s35, 6
	v_add_u32_e32 v7, s25, v15
	v_min_u32_e32 v7, 0xbf, v7
	v_lshlrev_b32_e32 v7, 2, v7
	v_add_u32_e32 v12, v1, v7
	v_add_u32_e32 v12, 0xf400, v12
	v_mul_u32_u24_e32 v9, 0x90, v13
	v_lshl_add_u32 v9, v14, 4, v9
	v_add_u32_e32 v9, v1, v9
	s_mul_i32 s25, s35, 0x900
	v_add_u32_e32 v11, s25, v9
	v_add_u32_e32 v11, 0xf800, v11
	v_and_b32_e32 v14, 1, v15
	v_lshlrev_b32_e32 v14, 3, v14
	v_sub_u32_e32 v9, v9, v14
	v_add_u32_e32 v10, s25, v9
	v_add_u32_e32 v10, 0xd000, v10
	s_mul_i32 s25, s35, 0x1200
	v_add_u32_e32 v9, s25, v9
	v_add_u32_e32 v9, 0x8800, v9
	v_lshrrev_b32_e32 v13, 4, v15
	v_mul_u32_u24_e32 v8, 0x110, v13
	v_and_b32_e32 v13, 15, v15
	v_lshl_add_u32 v8, v13, 4, v8
	v_sub_u32_e32 v8, v8, v14
	s_mul_i32 s25, s35, 0x1100
	v_add3_u32 v8, v8, v1, s25
	s_mov_b32 s3, 0
	s_mov_b32 s8, 0
	s_min_u32 s8, s8, 0x43
	s_cmp_lt_u32 s8, 4
	s_cselect_b32 s9, s43, s52
	s_mul_i32 s8, s42, s8
	s_add_i32 s8, s8, s9
	s_lshl_b32 s9, s8, 14
	s_add_u32 s46, s15, s9
	s_addc_u32 s47, s17, 0
	s_add_u32 s50, s13, s9
	s_addc_u32 s51, s14, 0
	s_add_u32 s10, s20, s9
	s_addc_u32 s11, s21, 0
	s_add_u32 s0, s31, s9
	s_addc_u32 s1, s36, 0
	s_mul_i32 s25, s8, 0x300
	s_add_u32 s40, s22, s25
	s_addc_u32 s41, s23, 0
	s_lshl_b32 s25, s8, 13
	s_add_u32 s8, s18, s25
	s_addc_u32 s9, s19, 0
	global_load_dwordx4 v[16:19], v4, s[46:47]
	global_load_dwordx4 v[32:35], v4, s[50:51]
	global_load_dwordx4 v[48:51], v4, s[10:11]
	global_load_dwordx4 v[20:23], v4, s[46:47] offset:1024
	global_load_dwordx4 v[36:39], v4, s[50:51] offset:1024
	global_load_dwordx4 v[52:55], v4, s[10:11] offset:1024
	global_load_dwordx4 v[24:27], v4, s[46:47] offset:2048
	global_load_dwordx4 v[40:43], v4, s[50:51] offset:2048
	global_load_dwordx4 v[56:59], v4, s[10:11] offset:2048
	global_load_dwordx4 v[28:31], v4, s[46:47] offset:3072
	global_load_dwordx4 v[44:47], v4, s[50:51] offset:3072
	global_load_dwordx4 v[60:63], v4, s[10:11] offset:3072
	global_load_dwordx4 v[64:67], v5, s[8:9]
	global_load_dwordx4 v[68:71], v5, s[8:9] offset:1024
	global_load_dwordx4 v[72:75], v6, s[0:1]
	global_load_dwordx4 v[76:79], v6, s[0:1] offset:2048
	global_load_dword v80, v7, s[40:41]
	s_mov_b32 s8, 1
	s_min_u32 s8, s8, 0x43
	s_cmp_lt_u32 s8, 4
	s_cselect_b32 s9, s43, s52
	s_mul_i32 s8, s42, s8
	s_add_i32 s8, s8, s9
	s_lshl_b32 s9, s8, 14
	s_add_u32 s46, s15, s9
	s_addc_u32 s47, s17, 0
	s_add_u32 s50, s13, s9
	s_addc_u32 s51, s14, 0
	s_add_u32 s10, s20, s9
	s_addc_u32 s11, s21, 0
	s_add_u32 s0, s31, s9
	s_addc_u32 s1, s36, 0
	s_mul_i32 s25, s8, 0x300
	s_add_u32 s40, s22, s25
	s_addc_u32 s41, s23, 0
	s_lshl_b32 s25, s8, 13
	s_add_u32 s8, s18, s25
	s_addc_u32 s9, s19, 0
	global_load_dwordx4 v[84:87], v4, s[46:47]
	global_load_dwordx4 v[100:103], v4, s[50:51]
	global_load_dwordx4 v[116:119], v4, s[10:11]
	global_load_dwordx4 v[88:91], v4, s[46:47] offset:1024
	global_load_dwordx4 v[104:107], v4, s[50:51] offset:1024
	global_load_dwordx4 v[120:123], v4, s[10:11] offset:1024
	global_load_dwordx4 v[92:95], v4, s[46:47] offset:2048
	global_load_dwordx4 v[108:111], v4, s[50:51] offset:2048
	global_load_dwordx4 v[124:127], v4, s[10:11] offset:2048
	global_load_dwordx4 v[96:99], v4, s[46:47] offset:3072
	global_load_dwordx4 v[112:115], v4, s[50:51] offset:3072
	global_load_dwordx4 v[128:131], v4, s[10:11] offset:3072
	global_load_dwordx4 v[132:135], v5, s[8:9]
	global_load_dwordx4 v[136:139], v5, s[8:9] offset:1024
	global_load_dwordx4 v[140:143], v6, s[0:1]
	global_load_dwordx4 v[144:147], v6, s[0:1] offset:2048
	global_load_dword v148, v7, s[40:41]
	s_mov_b32 s8, 2
	s_min_u32 s8, s8, 0x43
	s_cmp_lt_u32 s8, 4
	s_cselect_b32 s9, s43, s52
	s_mul_i32 s8, s42, s8
	s_add_i32 s8, s8, s9
	s_lshl_b32 s9, s8, 14
	s_add_u32 s46, s15, s9
	s_addc_u32 s47, s17, 0
	s_add_u32 s50, s13, s9
	s_addc_u32 s51, s14, 0
	s_add_u32 s10, s20, s9
	s_addc_u32 s11, s21, 0
	s_add_u32 s0, s31, s9
	s_addc_u32 s1, s36, 0
	s_mul_i32 s25, s8, 0x300
	s_add_u32 s40, s22, s25
	s_addc_u32 s41, s23, 0
	s_lshl_b32 s25, s8, 13
	s_add_u32 s8, s18, s25
	s_addc_u32 s9, s19, 0
	global_load_dwordx4 v[152:155], v4, s[46:47]
	global_load_dwordx4 v[168:171], v4, s[50:51]
	global_load_dwordx4 v[184:187], v4, s[10:11]
	global_load_dwordx4 v[156:159], v4, s[46:47] offset:1024
	global_load_dwordx4 v[172:175], v4, s[50:51] offset:1024
	global_load_dwordx4 v[188:191], v4, s[10:11] offset:1024
	global_load_dwordx4 v[160:163], v4, s[46:47] offset:2048
	global_load_dwordx4 v[176:179], v4, s[50:51] offset:2048
	global_load_dwordx4 v[192:195], v4, s[10:11] offset:2048
	global_load_dwordx4 v[164:167], v4, s[46:47] offset:3072
	global_load_dwordx4 v[180:183], v4, s[50:51] offset:3072
	global_load_dwordx4 v[196:199], v4, s[10:11] offset:3072
	global_load_dwordx4 v[200:203], v5, s[8:9]
	global_load_dwordx4 v[204:207], v5, s[8:9] offset:1024
	global_load_dwordx4 v[208:211], v6, s[0:1]
	global_load_dwordx4 v[212:215], v6, s[0:1] offset:2048
	global_load_dword v216, v7, s[40:41]
	v_mov_b32_e32 v13, v8
	s_waitcnt vmcnt(50)
	ds_write2_b64 v13, v[16:17], v[18:19] offset1:2
	v_add_u32_e32 v14, 0x4400, v8
	s_waitcnt vmcnt(49)
	ds_write2_b64 v14, v[32:33], v[34:35] offset1:2
	v_mov_b32_e32 v13, v9
	s_waitcnt vmcnt(48)
	ds_write2_b64 v13, v[48:49], v[50:51] offset1:2
	v_add_u32_e32 v14, 0x440, v8
	s_waitcnt vmcnt(47)
	ds_write2_b64 v14, v[20:21], v[22:23] offset1:2
	v_add_u32_e32 v13, 0x4840, v8
	s_waitcnt vmcnt(46)
	ds_write2_b64 v13, v[36:37], v[38:39] offset1:2
	v_add_u32_e32 v14, 0x480, v9
	s_waitcnt vmcnt(45)
	ds_write2_b64 v14, v[52:53], v[54:55] offset1:2
	v_add_u32_e32 v13, 0x880, v8
	s_waitcnt vmcnt(44)
	ds_write2_b64 v13, v[24:25], v[26:27] offset1:2
	v_add_u32_e32 v14, 0x4c80, v8
	s_waitcnt vmcnt(43)
	ds_write2_b64 v14, v[40:41], v[42:43] offset1:2
	v_add_u32_e32 v13, 0x900, v9
	s_waitcnt vmcnt(42)
	ds_write2_b64 v13, v[56:57], v[58:59] offset1:2
	v_add_u32_e32 v14, 0xcc0, v8
	s_waitcnt vmcnt(41)
	ds_write2_b64 v14, v[28:29], v[30:31] offset1:2
	v_add_u32_e32 v13, 0x50c0, v8
	s_waitcnt vmcnt(40)
	ds_write2_b64 v13, v[44:45], v[46:47] offset1:2
	v_add_u32_e32 v14, 0xd80, v9
	s_waitcnt vmcnt(39)
	ds_write2_b64 v14, v[60:61], v[62:63] offset1:2
	v_mov_b32_e32 v13, v10
	s_waitcnt vmcnt(38)
	ds_write2_b64 v13, v[64:65], v[66:67] offset1:2
	v_add_u32_e32 v14, 0x480, v10
	s_waitcnt vmcnt(37)
	ds_write2_b64 v14, v[68:69], v[70:71] offset1:2
	v_mov_b32_e32 v13, v11
	s_waitcnt vmcnt(36)
	ds_write_b128 v13, v[72:75]
	v_add_u32_e32 v14, 0x480, v11
	s_waitcnt vmcnt(35)
	ds_write_b128 v14, v[76:79]
	v_mov_b32_e32 v13, v12
	s_waitcnt vmcnt(34)
	ds_write_b32 v13, v80
	s_waitcnt lgkmcnt(0)
	s_mov_b32 s8, 3
	s_min_u32 s8, s8, 0x43
	s_cmp_lt_u32 s8, 4
	s_cselect_b32 s9, s43, s52
	s_mul_i32 s8, s42, s8
	s_add_i32 s8, s8, s9
	s_lshl_b32 s9, s8, 14
	s_add_u32 s46, s15, s9
	s_addc_u32 s47, s17, 0
	s_add_u32 s50, s13, s9
	s_addc_u32 s51, s14, 0
	s_add_u32 s10, s20, s9
	s_addc_u32 s11, s21, 0
	s_add_u32 s0, s31, s9
	s_addc_u32 s1, s36, 0
	s_mul_i32 s25, s8, 0x300
	s_add_u32 s40, s22, s25
	s_addc_u32 s41, s23, 0
	s_lshl_b32 s25, s8, 13
	s_add_u32 s8, s18, s25
	s_addc_u32 s9, s19, 0
	global_load_dwordx4 v[16:19], v4, s[46:47]
	global_load_dwordx4 v[32:35], v4, s[50:51]
	global_load_dwordx4 v[48:51], v4, s[10:11]
	global_load_dwordx4 v[20:23], v4, s[46:47] offset:1024
	global_load_dwordx4 v[36:39], v4, s[50:51] offset:1024
	global_load_dwordx4 v[52:55], v4, s[10:11] offset:1024
	global_load_dwordx4 v[24:27], v4, s[46:47] offset:2048
	global_load_dwordx4 v[40:43], v4, s[50:51] offset:2048
	global_load_dwordx4 v[56:59], v4, s[10:11] offset:2048
	global_load_dwordx4 v[28:31], v4, s[46:47] offset:3072
	global_load_dwordx4 v[44:47], v4, s[50:51] offset:3072
	global_load_dwordx4 v[60:63], v4, s[10:11] offset:3072
	global_load_dwordx4 v[64:67], v5, s[8:9]
	global_load_dwordx4 v[68:71], v5, s[8:9] offset:1024
	global_load_dwordx4 v[72:75], v6, s[0:1]
	global_load_dwordx4 v[76:79], v6, s[0:1] offset:2048
	global_load_dword v80, v7, s[40:41]
	s_barrier
.Lgs_loop:
	v_add_u32_e32 v13, 0x11c00, v8
	s_waitcnt vmcnt(50)
	ds_write2_b64 v13, v[84:85], v[86:87] offset1:2
	v_add_u32_e32 v14, 0x16000, v8
	s_waitcnt vmcnt(49)
	ds_write2_b64 v14, v[100:101], v[102:103] offset1:2
	v_add_u32_e32 v13, 0x11c00, v9
	s_waitcnt vmcnt(48)
	ds_write2_b64 v13, v[116:117], v[118:119] offset1:2
	v_add_u32_e32 v14, 0x12040, v8
	s_waitcnt vmcnt(47)
	ds_write2_b64 v14, v[88:89], v[90:91] offset1:2
	v_add_u32_e32 v13, 0x16440, v8
	s_waitcnt vmcnt(46)
	ds_write2_b64 v13, v[104:105], v[106:107] offset1:2
	v_add_u32_e32 v14, 0x12080, v9
	s_waitcnt vmcnt(45)
	ds_write2_b64 v14, v[120:121], v[122:123] offset1:2
	v_add_u32_e32 v13, 0x12480, v8
	s_waitcnt vmcnt(44)
	ds_write2_b64 v13, v[92:93], v[94:95] offset1:2
	v_add_u32_e32 v14, 0x16880, v8
	s_waitcnt vmcnt(43)
	ds_write2_b64 v14, v[108:109], v[110:111] offset1:2
	v_add_u32_e32 v13, 0x12500, v9
	s_waitcnt vmcnt(42)
	ds_write2_b64 v13, v[124:125], v[126:127] offset1:2
	v_add_u32_e32 v14, 0x128c0, v8
	s_waitcnt vmcnt(41)
	ds_write2_b64 v14, v[96:97], v[98:99] offset1:2
	v_add_u32_e32 v13, 0x16cc0, v8
	s_waitcnt vmcnt(40)
	ds_write2_b64 v13, v[112:113], v[114:115] offset1:2
	v_add_u32_e32 v14, 0x12980, v9
	s_waitcnt vmcnt(39)
	ds_write2_b64 v14, v[128:129], v[130:131] offset1:2
	v_add_u32_e32 v13, 0x11c00, v10
	s_waitcnt vmcnt(38)
	ds_write2_b64 v13, v[132:133], v[134:135] offset1:2
	v_add_u32_e32 v14, 0x12080, v10
	s_waitcnt vmcnt(37)
	ds_write2_b64 v14, v[136:137], v[138:139] offset1:2
	v_add_u32_e32 v13, 0x11c00, v11
	s_waitcnt vmcnt(36)
	ds_write_b128 v13, v[140:143]
	v_add_u32_e32 v14, 0x12080, v11
	s_waitcnt vmcnt(35)
	ds_write_b128 v14, v[144:147]
	v_add_u32_e32 v13, 0x11c00, v12
	s_waitcnt vmcnt(34)
	ds_write_b32 v13, v148
	s_waitcnt lgkmcnt(0)
	s_add_i32 s8, s3, 4
	s_min_u32 s8, s8, 0x43
	s_cmp_lt_u32 s8, 4
	s_cselect_b32 s9, s43, s52
	s_mul_i32 s8, s42, s8
	s_add_i32 s8, s8, s9
	s_lshl_b32 s9, s8, 14
	s_add_u32 s46, s15, s9
	s_addc_u32 s47, s17, 0
	s_add_u32 s50, s13, s9
	s_addc_u32 s51, s14, 0
	s_add_u32 s10, s20, s9
	s_addc_u32 s11, s21, 0
	s_add_u32 s0, s31, s9
	s_addc_u32 s1, s36, 0
	s_mul_i32 s25, s8, 0x300
	s_add_u32 s40, s22, s25
	s_addc_u32 s41, s23, 0
	s_lshl_b32 s25, s8, 13
	s_add_u32 s8, s18, s25
	s_addc_u32 s9, s19, 0
	global_load_dwordx4 v[84:87], v4, s[46:47]
	global_load_dwordx4 v[100:103], v4, s[50:51]
	global_load_dwordx4 v[116:119], v4, s[10:11]
	global_load_dwordx4 v[88:91], v4, s[46:47] offset:1024
	global_load_dwordx4 v[104:107], v4, s[50:51] offset:1024
	global_load_dwordx4 v[120:123], v4, s[10:11] offset:1024
	global_load_dwordx4 v[92:95], v4, s[46:47] offset:2048
	global_load_dwordx4 v[108:111], v4, s[50:51] offset:2048
	global_load_dwordx4 v[124:127], v4, s[10:11] offset:2048
	global_load_dwordx4 v[96:99], v4, s[46:47] offset:3072
	global_load_dwordx4 v[112:115], v4, s[50:51] offset:3072
	global_load_dwordx4 v[128:131], v4, s[10:11] offset:3072
	global_load_dwordx4 v[132:135], v5, s[8:9]
	global_load_dwordx4 v[136:139], v5, s[8:9] offset:1024
	global_load_dwordx4 v[140:143], v6, s[0:1]
	global_load_dwordx4 v[144:147], v6, s[0:1] offset:2048
	global_load_dword v148, v7, s[40:41]
	s_barrier
	s_add_i32 s3, s3, 1
	s_cmp_eq_u32 s3, 0x44
	s_cbranch_scc1 .Lgs_done
	v_mov_b32_e32 v13, v8
	s_waitcnt vmcnt(50)
	ds_write2_b64 v13, v[152:153], v[154:155] offset1:2
	v_add_u32_e32 v14, 0x4400, v8
	s_waitcnt vmcnt(49)
	ds_write2_b64 v14, v[168:169], v[170:171] offset1:2
	v_mov_b32_e32 v13, v9
	s_waitcnt vmcnt(48)
	ds_write2_b64 v13, v[184:185], v[186:187] offset1:2
	v_add_u32_e32 v14, 0x440, v8
	s_waitcnt vmcnt(47)
	ds_write2_b64 v14, v[156:157], v[158:159] offset1:2
	v_add_u32_e32 v13, 0x4840, v8
	s_waitcnt vmcnt(46)
	ds_write2_b64 v13, v[172:173], v[174:175] offset1:2
	v_add_u32_e32 v14, 0x480, v9
	s_waitcnt vmcnt(45)
	ds_write2_b64 v14, v[188:189], v[190:191] offset1:2
	v_add_u32_e32 v13, 0x880, v8
	s_waitcnt vmcnt(44)
	ds_write2_b64 v13, v[160:161], v[162:163] offset1:2
	v_add_u32_e32 v14, 0x4c80, v8
	s_waitcnt vmcnt(43)
	ds_write2_b64 v14, v[176:177], v[178:179] offset1:2
	v_add_u32_e32 v13, 0x900, v9
	s_waitcnt vmcnt(42)
	ds_write2_b64 v13, v[192:193], v[194:195] offset1:2
	v_add_u32_e32 v14, 0xcc0, v8
	s_waitcnt vmcnt(41)
	ds_write2_b64 v14, v[164:165], v[166:167] offset1:2
	v_add_u32_e32 v13, 0x50c0, v8
	s_waitcnt vmcnt(40)
	ds_write2_b64 v13, v[180:181], v[182:183] offset1:2
	v_add_u32_e32 v14, 0xd80, v9
	s_waitcnt vmcnt(39)
	ds_write2_b64 v14, v[196:197], v[198:199] offset1:2
	v_mov_b32_e32 v13, v10
	s_waitcnt vmcnt(38)
	ds_write2_b64 v13, v[200:201], v[202:203] offset1:2
	v_add_u32_e32 v14, 0x480, v10
	s_waitcnt vmcnt(37)
	ds_write2_b64 v14, v[204:205], v[206:207] offset1:2
	v_mov_b32_e32 v13, v11
	s_waitcnt vmcnt(36)
	ds_write_b128 v13, v[208:211]
	v_add_u32_e32 v14, 0x480, v11
	s_waitcnt vmcnt(35)
	ds_write_b128 v14, v[212:215]
	v_mov_b32_e32 v13, v12
	s_waitcnt vmcnt(34)
	ds_write_b32 v13, v216
	s_waitcnt lgkmcnt(0)
	s_add_i32 s8, s3, 4
	s_min_u32 s8, s8, 0x43
	s_cmp_lt_u32 s8, 4
	s_cselect_b32 s9, s43, s52
	s_mul_i32 s8, s42, s8
	s_add_i32 s8, s8, s9
	s_lshl_b32 s9, s8, 14
	s_add_u32 s46, s15, s9
	s_addc_u32 s47, s17, 0
	s_add_u32 s50, s13, s9
	s_addc_u32 s51, s14, 0
	s_add_u32 s10, s20, s9
	s_addc_u32 s11, s21, 0
	s_add_u32 s0, s31, s9
	s_addc_u32 s1, s36, 0
	s_mul_i32 s25, s8, 0x300
	s_add_u32 s40, s22, s25
	s_addc_u32 s41, s23, 0
	s_lshl_b32 s25, s8, 13
	s_add_u32 s8, s18, s25
	s_addc_u32 s9, s19, 0
	global_load_dwordx4 v[152:155], v4, s[46:47]
	global_load_dwordx4 v[168:171], v4, s[50:51]
	global_load_dwordx4 v[184:187], v4, s[10:11]
	global_load_dwordx4 v[156:159], v4, s[46:47] offset:1024
	global_load_dwordx4 v[172:175], v4, s[50:51] offset:1024
	global_load_dwordx4 v[188:191], v4, s[10:11] offset:1024
	global_load_dwordx4 v[160:163], v4, s[46:47] offset:2048
	global_load_dwordx4 v[176:179], v4, s[50:51] offset:2048
	global_load_dwordx4 v[192:195], v4, s[10:11] offset:2048
	global_load_dwordx4 v[164:167], v4, s[46:47] offset:3072
	global_load_dwordx4 v[180:183], v4, s[50:51] offset:3072
	global_load_dwordx4 v[196:199], v4, s[10:11] offset:3072
	global_load_dwordx4 v[200:203], v5, s[8:9]
	global_load_dwordx4 v[204:207], v5, s[8:9] offset:1024
	global_load_dwordx4 v[208:211], v6, s[0:1]
	global_load_dwordx4 v[212:215], v6, s[0:1] offset:2048
	global_load_dword v216, v7, s[40:41]
	s_barrier
	s_add_i32 s3, s3, 1
	s_cmp_eq_u32 s3, 0x44
	s_cbranch_scc1 .Lgs_done
	v_add_u32_e32 v13, 0x11c00, v8
	s_waitcnt vmcnt(50)
	ds_write2_b64 v13, v[16:17], v[18:19] offset1:2
	v_add_u32_e32 v14, 0x16000, v8
	s_waitcnt vmcnt(49)
	ds_write2_b64 v14, v[32:33], v[34:35] offset1:2
	v_add_u32_e32 v13, 0x11c00, v9
	s_waitcnt vmcnt(48)
	ds_write2_b64 v13, v[48:49], v[50:51] offset1:2
	v_add_u32_e32 v14, 0x12040, v8
	s_waitcnt vmcnt(47)
	ds_write2_b64 v14, v[20:21], v[22:23] offset1:2
	v_add_u32_e32 v13, 0x16440, v8
	s_waitcnt vmcnt(46)
	ds_write2_b64 v13, v[36:37], v[38:39] offset1:2
	v_add_u32_e32 v14, 0x12080, v9
	s_waitcnt vmcnt(45)
	ds_write2_b64 v14, v[52:53], v[54:55] offset1:2
	v_add_u32_e32 v13, 0x12480, v8
	s_waitcnt vmcnt(44)
	ds_write2_b64 v13, v[24:25], v[26:27] offset1:2
	v_add_u32_e32 v14, 0x16880, v8
	s_waitcnt vmcnt(43)
	ds_write2_b64 v14, v[40:41], v[42:43] offset1:2
	v_add_u32_e32 v13, 0x12500, v9
	s_waitcnt vmcnt(42)
	ds_write2_b64 v13, v[56:57], v[58:59] offset1:2
	v_add_u32_e32 v14, 0x128c0, v8
	s_waitcnt vmcnt(41)
	ds_write2_b64 v14, v[28:29], v[30:31] offset1:2
	v_add_u32_e32 v13, 0x16cc0, v8
	s_waitcnt vmcnt(40)
	ds_write2_b64 v13, v[44:45], v[46:47] offset1:2
	v_add_u32_e32 v14, 0x12980, v9
	s_waitcnt vmcnt(39)
	ds_write2_b64 v14, v[60:61], v[62:63] offset1:2
	v_add_u32_e32 v13, 0x11c00, v10
	s_waitcnt vmcnt(38)
	ds_write2_b64 v13, v[64:65], v[66:67] offset1:2
	v_add_u32_e32 v14, 0x12080, v10
	s_waitcnt vmcnt(37)
	ds_write2_b64 v14, v[68:69], v[70:71] offset1:2
	v_add_u32_e32 v13, 0x11c00, v11
	s_waitcnt vmcnt(36)
	ds_write_b128 v13, v[72:75]
	v_add_u32_e32 v14, 0x12080, v11
	s_waitcnt vmcnt(35)
	ds_write_b128 v14, v[76:79]
	v_add_u32_e32 v13, 0x11c00, v12
	s_waitcnt vmcnt(34)
	ds_write_b32 v13, v80
	s_waitcnt lgkmcnt(0)
	s_add_i32 s8, s3, 4
	s_min_u32 s8, s8, 0x43
	s_cmp_lt_u32 s8, 4
	s_cselect_b32 s9, s43, s52
	s_mul_i32 s8, s42, s8
	s_add_i32 s8, s8, s9
	s_lshl_b32 s9, s8, 14
	s_add_u32 s46, s15, s9
	s_addc_u32 s47, s17, 0
	s_add_u32 s50, s13, s9
	s_addc_u32 s51, s14, 0
	s_add_u32 s10, s20, s9
	s_addc_u32 s11, s21, 0
	s_add_u32 s0, s31, s9
	s_addc_u32 s1, s36, 0
	s_mul_i32 s25, s8, 0x300
	s_add_u32 s40, s22, s25
	s_addc_u32 s41, s23, 0
	s_lshl_b32 s25, s8, 13
	s_add_u32 s8, s18, s25
	s_addc_u32 s9, s19, 0
	global_load_dwordx4 v[16:19], v4, s[46:47]
	global_load_dwordx4 v[32:35], v4, s[50:51]
	global_load_dwordx4 v[48:51], v4, s[10:11]
	global_load_dwordx4 v[20:23], v4, s[46:47] offset:1024
	global_load_dwordx4 v[36:39], v4, s[50:51] offset:1024
	global_load_dwordx4 v[52:55], v4, s[10:11] offset:1024
	global_load_dwordx4 v[24:27], v4, s[46:47] offset:2048
	global_load_dwordx4 v[40:43], v4, s[50:51] offset:2048
	global_load_dwordx4 v[56:59], v4, s[10:11] offset:2048
	global_load_dwordx4 v[28:31], v4, s[46:47] offset:3072
	global_load_dwordx4 v[44:47], v4, s[50:51] offset:3072
	global_load_dwordx4 v[60:63], v4, s[10:11] offset:3072
	global_load_dwordx4 v[64:67], v5, s[8:9]
	global_load_dwordx4 v[68:71], v5, s[8:9] offset:1024
	global_load_dwordx4 v[72:75], v6, s[0:1]
	global_load_dwordx4 v[76:79], v6, s[0:1] offset:2048
	global_load_dword v80, v7, s[40:41]
	s_barrier
	s_add_i32 s3, s3, 1
	s_cmp_eq_u32 s3, 0x44
	s_cbranch_scc1 .Lgs_done
	v_mov_b32_e32 v13, v8
	s_waitcnt vmcnt(50)
	ds_write2_b64 v13, v[84:85], v[86:87] offset1:2
	v_add_u32_e32 v14, 0x4400, v8
	s_waitcnt vmcnt(49)
	ds_write2_b64 v14, v[100:101], v[102:103] offset1:2
	v_mov_b32_e32 v13, v9
	s_waitcnt vmcnt(48)
	ds_write2_b64 v13, v[116:117], v[118:119] offset1:2
	v_add_u32_e32 v14, 0x440, v8
	s_waitcnt vmcnt(47)
	ds_write2_b64 v14, v[88:89], v[90:91] offset1:2
	v_add_u32_e32 v13, 0x4840, v8
	s_waitcnt vmcnt(46)
	ds_write2_b64 v13, v[104:105], v[106:107] offset1:2
	v_add_u32_e32 v14, 0x480, v9
	s_waitcnt vmcnt(45)
	ds_write2_b64 v14, v[120:121], v[122:123] offset1:2
	v_add_u32_e32 v13, 0x880, v8
	s_waitcnt vmcnt(44)
	ds_write2_b64 v13, v[92:93], v[94:95] offset1:2
	v_add_u32_e32 v14, 0x4c80, v8
	s_waitcnt vmcnt(43)
	ds_write2_b64 v14, v[108:109], v[110:111] offset1:2
	v_add_u32_e32 v13, 0x900, v9
	s_waitcnt vmcnt(42)
	ds_write2_b64 v13, v[124:125], v[126:127] offset1:2
	v_add_u32_e32 v14, 0xcc0, v8
	s_waitcnt vmcnt(41)
	ds_write2_b64 v14, v[96:97], v[98:99] offset1:2
	v_add_u32_e32 v13, 0x50c0, v8
	s_waitcnt vmcnt(40)
	ds_write2_b64 v13, v[112:113], v[114:115] offset1:2
	v_add_u32_e32 v14, 0xd80, v9
	s_waitcnt vmcnt(39)
	ds_write2_b64 v14, v[128:129], v[130:131] offset1:2
	v_mov_b32_e32 v13, v10
	s_waitcnt vmcnt(38)
	ds_write2_b64 v13, v[132:133], v[134:135] offset1:2
	v_add_u32_e32 v14, 0x480, v10
	s_waitcnt vmcnt(37)
	ds_write2_b64 v14, v[136:137], v[138:139] offset1:2
	v_mov_b32_e32 v13, v11
	s_waitcnt vmcnt(36)
	ds_write_b128 v13, v[140:143]
	v_add_u32_e32 v14, 0x480, v11
	s_waitcnt vmcnt(35)
	ds_write_b128 v14, v[144:147]
	v_mov_b32_e32 v13, v12
	s_waitcnt vmcnt(34)
	ds_write_b32 v13, v148
	s_waitcnt lgkmcnt(0)
	s_add_i32 s8, s3, 4
	s_min_u32 s8, s8, 0x43
	s_cmp_lt_u32 s8, 4
	s_cselect_b32 s9, s43, s52
	s_mul_i32 s8, s42, s8
	s_add_i32 s8, s8, s9
	s_lshl_b32 s9, s8, 14
	s_add_u32 s46, s15, s9
	s_addc_u32 s47, s17, 0
	s_add_u32 s50, s13, s9
	s_addc_u32 s51, s14, 0
	s_add_u32 s10, s20, s9
	s_addc_u32 s11, s21, 0
	s_add_u32 s0, s31, s9
	s_addc_u32 s1, s36, 0
	s_mul_i32 s25, s8, 0x300
	s_add_u32 s40, s22, s25
	s_addc_u32 s41, s23, 0
	s_lshl_b32 s25, s8, 13
	s_add_u32 s8, s18, s25
	s_addc_u32 s9, s19, 0
	global_load_dwordx4 v[84:87], v4, s[46:47]
	global_load_dwordx4 v[100:103], v4, s[50:51]
	global_load_dwordx4 v[116:119], v4, s[10:11]
	global_load_dwordx4 v[88:91], v4, s[46:47] offset:1024
	global_load_dwordx4 v[104:107], v4, s[50:51] offset:1024
	global_load_dwordx4 v[120:123], v4, s[10:11] offset:1024
	global_load_dwordx4 v[92:95], v4, s[46:47] offset:2048
	global_load_dwordx4 v[108:111], v4, s[50:51] offset:2048
	global_load_dwordx4 v[124:127], v4, s[10:11] offset:2048
	global_load_dwordx4 v[96:99], v4, s[46:47] offset:3072
	global_load_dwordx4 v[112:115], v4, s[50:51] offset:3072
	global_load_dwordx4 v[128:131], v4, s[10:11] offset:3072
	global_load_dwordx4 v[132:135], v5, s[8:9]
	global_load_dwordx4 v[136:139], v5, s[8:9] offset:1024
	global_load_dwordx4 v[140:143], v6, s[0:1]
	global_load_dwordx4 v[144:147], v6, s[0:1] offset:2048
	global_load_dword v148, v7, s[40:41]
	s_barrier
	s_add_i32 s3, s3, 1
	s_cmp_eq_u32 s3, 0x44
	s_cbranch_scc1 .Lgs_done
	v_add_u32_e32 v13, 0x11c00, v8
	s_waitcnt vmcnt(50)
	ds_write2_b64 v13, v[152:153], v[154:155] offset1:2
	v_add_u32_e32 v14, 0x16000, v8
	s_waitcnt vmcnt(49)
	ds_write2_b64 v14, v[168:169], v[170:171] offset1:2
	v_add_u32_e32 v13, 0x11c00, v9
	s_waitcnt vmcnt(48)
	ds_write2_b64 v13, v[184:185], v[186:187] offset1:2
	v_add_u32_e32 v14, 0x12040, v8
	s_waitcnt vmcnt(47)
	ds_write2_b64 v14, v[156:157], v[158:159] offset1:2
	v_add_u32_e32 v13, 0x16440, v8
	s_waitcnt vmcnt(46)
	ds_write2_b64 v13, v[172:173], v[174:175] offset1:2
	v_add_u32_e32 v14, 0x12080, v9
	s_waitcnt vmcnt(45)
	ds_write2_b64 v14, v[188:189], v[190:191] offset1:2
	v_add_u32_e32 v13, 0x12480, v8
	s_waitcnt vmcnt(44)
	ds_write2_b64 v13, v[160:161], v[162:163] offset1:2
	v_add_u32_e32 v14, 0x16880, v8
	s_waitcnt vmcnt(43)
	ds_write2_b64 v14, v[176:177], v[178:179] offset1:2
	v_add_u32_e32 v13, 0x12500, v9
	s_waitcnt vmcnt(42)
	ds_write2_b64 v13, v[192:193], v[194:195] offset1:2
	v_add_u32_e32 v14, 0x128c0, v8
	s_waitcnt vmcnt(41)
	ds_write2_b64 v14, v[164:165], v[166:167] offset1:2
	v_add_u32_e32 v13, 0x16cc0, v8
	s_waitcnt vmcnt(40)
	ds_write2_b64 v13, v[180:181], v[182:183] offset1:2
	v_add_u32_e32 v14, 0x12980, v9
	s_waitcnt vmcnt(39)
	ds_write2_b64 v14, v[196:197], v[198:199] offset1:2
	v_add_u32_e32 v13, 0x11c00, v10
	s_waitcnt vmcnt(38)
	ds_write2_b64 v13, v[200:201], v[202:203] offset1:2
	v_add_u32_e32 v14, 0x12080, v10
	s_waitcnt vmcnt(37)
	ds_write2_b64 v14, v[204:205], v[206:207] offset1:2
	v_add_u32_e32 v13, 0x11c00, v11
	s_waitcnt vmcnt(36)
	ds_write_b128 v13, v[208:211]
	v_add_u32_e32 v14, 0x12080, v11
	s_waitcnt vmcnt(35)
	ds_write_b128 v14, v[212:215]
	v_add_u32_e32 v13, 0x11c00, v12
	s_waitcnt vmcnt(34)
	ds_write_b32 v13, v216
	s_waitcnt lgkmcnt(0)
	s_add_i32 s8, s3, 4
	s_min_u32 s8, s8, 0x43
	s_cmp_lt_u32 s8, 4
	s_cselect_b32 s9, s43, s52
	s_mul_i32 s8, s42, s8
	s_add_i32 s8, s8, s9
	s_lshl_b32 s9, s8, 14
	s_add_u32 s46, s15, s9
	s_addc_u32 s47, s17, 0
	s_add_u32 s50, s13, s9
	s_addc_u32 s51, s14, 0
	s_add_u32 s10, s20, s9
	s_addc_u32 s11, s21, 0
	s_add_u32 s0, s31, s9
	s_addc_u32 s1, s36, 0
	s_mul_i32 s25, s8, 0x300
	s_add_u32 s40, s22, s25
	s_addc_u32 s41, s23, 0
	s_lshl_b32 s25, s8, 13
	s_add_u32 s8, s18, s25
	s_addc_u32 s9, s19, 0
	global_load_dwordx4 v[152:155], v4, s[46:47]
	global_load_dwordx4 v[168:171], v4, s[50:51]
	global_load_dwordx4 v[184:187], v4, s[10:11]
	global_load_dwordx4 v[156:159], v4, s[46:47] offset:1024
	global_load_dwordx4 v[172:175], v4, s[50:51] offset:1024
	global_load_dwordx4 v[188:191], v4, s[10:11] offset:1024
	global_load_dwordx4 v[160:163], v4, s[46:47] offset:2048
	global_load_dwordx4 v[176:179], v4, s[50:51] offset:2048
	global_load_dwordx4 v[192:195], v4, s[10:11] offset:2048
	global_load_dwordx4 v[164:167], v4, s[46:47] offset:3072
	global_load_dwordx4 v[180:183], v4, s[50:51] offset:3072
	global_load_dwordx4 v[196:199], v4, s[10:11] offset:3072
	global_load_dwordx4 v[200:203], v5, s[8:9]
	global_load_dwordx4 v[204:207], v5, s[8:9] offset:1024
	global_load_dwordx4 v[208:211], v6, s[0:1]
	global_load_dwordx4 v[212:215], v6, s[0:1] offset:2048
	global_load_dword v216, v7, s[40:41]
	s_barrier
	s_add_i32 s3, s3, 1
	s_cmp_eq_u32 s3, 0x44
	s_cbranch_scc1 .Lgs_done
	v_mov_b32_e32 v13, v8
	s_waitcnt vmcnt(50)
	ds_write2_b64 v13, v[16:17], v[18:19] offset1:2
	v_add_u32_e32 v14, 0x4400, v8
	s_waitcnt vmcnt(49)
	ds_write2_b64 v14, v[32:33], v[34:35] offset1:2
	v_mov_b32_e32 v13, v9
	s_waitcnt vmcnt(48)
	ds_write2_b64 v13, v[48:49], v[50:51] offset1:2
	v_add_u32_e32 v14, 0x440, v8
	s_waitcnt vmcnt(47)
	ds_write2_b64 v14, v[20:21], v[22:23] offset1:2
	v_add_u32_e32 v13, 0x4840, v8
	s_waitcnt vmcnt(46)
	ds_write2_b64 v13, v[36:37], v[38:39] offset1:2
	v_add_u32_e32 v14, 0x480, v9
	s_waitcnt vmcnt(45)
	ds_write2_b64 v14, v[52:53], v[54:55] offset1:2
	v_add_u32_e32 v13, 0x880, v8
	s_waitcnt vmcnt(44)
	ds_write2_b64 v13, v[24:25], v[26:27] offset1:2
	v_add_u32_e32 v14, 0x4c80, v8
	s_waitcnt vmcnt(43)
	ds_write2_b64 v14, v[40:41], v[42:43] offset1:2
	v_add_u32_e32 v13, 0x900, v9
	s_waitcnt vmcnt(42)
	ds_write2_b64 v13, v[56:57], v[58:59] offset1:2
	v_add_u32_e32 v14, 0xcc0, v8
	s_waitcnt vmcnt(41)
	ds_write2_b64 v14, v[28:29], v[30:31] offset1:2
	v_add_u32_e32 v13, 0x50c0, v8
	s_waitcnt vmcnt(40)
	ds_write2_b64 v13, v[44:45], v[46:47] offset1:2
	v_add_u32_e32 v14, 0xd80, v9
	s_waitcnt vmcnt(39)
	ds_write2_b64 v14, v[60:61], v[62:63] offset1:2
	v_mov_b32_e32 v13, v10
	s_waitcnt vmcnt(38)
	ds_write2_b64 v13, v[64:65], v[66:67] offset1:2
	v_add_u32_e32 v14, 0x480, v10
	s_waitcnt vmcnt(37)
	ds_write2_b64 v14, v[68:69], v[70:71] offset1:2
	v_mov_b32_e32 v13, v11
	s_waitcnt vmcnt(36)
	ds_write_b128 v13, v[72:75]
	v_add_u32_e32 v14, 0x480, v11
	s_waitcnt vmcnt(35)
	ds_write_b128 v14, v[76:79]
	v_mov_b32_e32 v13, v12
	s_waitcnt vmcnt(34)
	ds_write_b32 v13, v80
	s_waitcnt lgkmcnt(0)
	s_add_i32 s8, s3, 4
	s_min_u32 s8, s8, 0x43
	s_cmp_lt_u32 s8, 4
	s_cselect_b32 s9, s43, s52
	s_mul_i32 s8, s42, s8
	s_add_i32 s8, s8, s9
	s_lshl_b32 s9, s8, 14
	s_add_u32 s46, s15, s9
	s_addc_u32 s47, s17, 0
	s_add_u32 s50, s13, s9
	s_addc_u32 s51, s14, 0
	s_add_u32 s10, s20, s9
	s_addc_u32 s11, s21, 0
	s_add_u32 s0, s31, s9
	s_addc_u32 s1, s36, 0
	s_mul_i32 s25, s8, 0x300
	s_add_u32 s40, s22, s25
	s_addc_u32 s41, s23, 0
	s_lshl_b32 s25, s8, 13
	s_add_u32 s8, s18, s25
	s_addc_u32 s9, s19, 0
	global_load_dwordx4 v[16:19], v4, s[46:47]
	global_load_dwordx4 v[32:35], v4, s[50:51]
	global_load_dwordx4 v[48:51], v4, s[10:11]
	global_load_dwordx4 v[20:23], v4, s[46:47] offset:1024
	global_load_dwordx4 v[36:39], v4, s[50:51] offset:1024
	global_load_dwordx4 v[52:55], v4, s[10:11] offset:1024
	global_load_dwordx4 v[24:27], v4, s[46:47] offset:2048
	global_load_dwordx4 v[40:43], v4, s[50:51] offset:2048
	global_load_dwordx4 v[56:59], v4, s[10:11] offset:2048
	global_load_dwordx4 v[28:31], v4, s[46:47] offset:3072
	global_load_dwordx4 v[44:47], v4, s[50:51] offset:3072
	global_load_dwordx4 v[60:63], v4, s[10:11] offset:3072
	global_load_dwordx4 v[64:67], v5, s[8:9]
	global_load_dwordx4 v[68:71], v5, s[8:9] offset:1024
	global_load_dwordx4 v[72:75], v6, s[0:1]
	global_load_dwordx4 v[76:79], v6, s[0:1] offset:2048
	global_load_dword v80, v7, s[40:41]
	s_barrier
	s_add_i32 s3, s3, 1
	s_cmp_eq_u32 s3, 0x44
	s_cbranch_scc1 .Lgs_done
	s_branch .Lgs_loop
.Lgs_done:
	s_waitcnt vmcnt(0)
	v_mov_b32_e32 v134, 0x3ecc95a3
	s_branch .LBB0_1626
